# speedup vs baseline: 1.0304x; 1.0304x over previous
.Lg_loop:
	v_add_u32_e32 v6, s33, v5
	ds_read_b128 v[72:75], v6 offset:0
	ds_read_b128 v[76:79], v6 offset:2048
	ds_read_b128 v[80:83], v6 offset:4096
	ds_read_b128 v[84:87], v6 offset:6144
	ds_read_b128 v[88:91], v4 offset:0
	ds_read_b128 v[92:95], v4 offset:2048
	ds_read_b128 v[96:99], v4 offset:4096
	ds_read_b128 v[100:103], v4 offset:6144
	ds_read_b128 v[104:107], v4 offset:8192
	ds_read_b128 v[108:111], v4 offset:10240
	ds_read_b128 v[112:115], v4 offset:12288
	ds_read_b128 v[116:119], v4 offset:14336
	s_waitcnt vmcnt(18)
	v_cvt_pk_bf16_f32 v40, v40, v41
	v_cvt_pk_bf16_f32 v41, v42, v43
	v_cvt_pk_bf16_f32 v44, v44, v45
	v_cvt_pk_bf16_f32 v45, v46, v47
	ds_write2st64_b64 v3, v[40:41], v[44:45] offset0:64 offset1:72
	s_waitcnt vmcnt(16)
	v_cvt_pk_bf16_f32 v48, v48, v49
	v_cvt_pk_bf16_f32 v49, v50, v51
	v_cvt_pk_bf16_f32 v52, v52, v53
	v_cvt_pk_bf16_f32 v53, v54, v55
	ds_write2st64_b64 v3, v[48:49], v[52:53] offset0:80 offset1:88
	s_waitcnt lgkmcnt(0)
	s_barrier
	s_setprio 1
	s_mov_b32 m0, s26
	s_min_u32 s40, s25, 31
	s_bitcmp1_b32 s40, 4
	s_cselect_b32 s41, s23, s22
	s_lshl_b32 s42, s40, 23
	s_and_b32 s42, s42, 0x7000000
	s_or_b32 s41, s41, s42
	s_lshl_b32 s42, s40, 8
	s_and_b32 s42, s42, 0x100
	s_or_b32 s41, s41, s42
	s_sub_u32 s43, s25, 1
	s_min_u32 s43, s43, 31
	s_and_b32 s43, s43, 15
	s_lshl_b32 s43, s43, 15
	s_add_u32 s44, s43, s24
	v_mfma_f32_16x16x32_bf16 v[120:123], v[72:75], v[88:91], v[120:123]
	v_mfma_f32_16x16x32_bf16 v[124:127], v[76:79], v[88:91], v[124:127]
	buffer_load_dwordx4 v2, s[12:15], s44 offen sc1 lds
	v_mfma_f32_16x16x32_bf16 v[128:131], v[80:83], v[88:91], v[128:131]
	v_mfma_f32_16x16x32_bf16 v[132:135], v[84:87], v[88:91], v[132:135]
	buffer_load_dwordx4 v2, s[12:15], s44 offen offset:1024 sc1 lds
	v_mfma_f32_16x16x32_bf16 v[136:139], v[72:75], v[92:95], v[136:139]
	v_mfma_f32_16x16x32_bf16 v[140:143], v[76:79], v[92:95], v[140:143]
	buffer_load_dwordx4 v2, s[12:15], s44 offen offset:2048 sc1 lds
	v_mfma_f32_16x16x32_bf16 v[144:147], v[80:83], v[92:95], v[144:147]
	v_mfma_f32_16x16x32_bf16 v[148:151], v[84:87], v[92:95], v[148:151]
	buffer_load_dwordx4 v2, s[12:15], s44 offen offset:3072 sc1 lds
	v_mfma_f32_16x16x32_bf16 v[152:155], v[72:75], v[96:99], v[152:155]
	v_mfma_f32_16x16x32_bf16 v[156:159], v[76:79], v[96:99], v[156:159]
	v_mfma_f32_16x16x32_bf16 v[160:163], v[80:83], v[96:99], v[160:163]
	v_mfma_f32_16x16x32_bf16 v[164:167], v[84:87], v[96:99], v[164:167]
	buffer_load_dwordx4 v[40:43], v1, s[4:7], s41 offen sc0 nt
	v_mfma_f32_16x16x32_bf16 v[168:171], v[72:75], v[100:103], v[168:171]
	v_mfma_f32_16x16x32_bf16 v[172:175], v[76:79], v[100:103], v[172:175]
	v_mfma_f32_16x16x32_bf16 v[176:179], v[80:83], v[100:103], v[176:179]
	v_mfma_f32_16x16x32_bf16 v[180:183], v[84:87], v[100:103], v[180:183]
	s_add_u32 s42, s41, 0x4000
	buffer_load_dwordx4 v[44:47], v1, s[4:7], s42 offen sc0 nt
	v_mfma_f32_16x16x32_bf16 v[184:187], v[72:75], v[104:107], v[184:187]
	v_mfma_f32_16x16x32_bf16 v[188:191], v[76:79], v[104:107], v[188:191]
	v_mfma_f32_16x16x32_bf16 v[192:195], v[80:83], v[104:107], v[192:195]
	v_mfma_f32_16x16x32_bf16 v[196:199], v[84:87], v[104:107], v[196:199]
	s_add_u32 s42, s41, 0x8000
	buffer_load_dwordx4 v[48:51], v1, s[4:7], s42 offen sc0 nt
	v_mfma_f32_16x16x32_bf16 v[200:203], v[72:75], v[108:111], v[200:203]
	v_mfma_f32_16x16x32_bf16 v[204:207], v[76:79], v[108:111], v[204:207]
	v_mfma_f32_16x16x32_bf16 v[208:211], v[80:83], v[108:111], v[208:211]
	v_mfma_f32_16x16x32_bf16 v[212:215], v[84:87], v[108:111], v[212:215]
	s_add_u32 s42, s41, 0xc000
	buffer_load_dwordx4 v[52:55], v1, s[4:7], s42 offen sc0 nt
	v_mfma_f32_16x16x32_bf16 v[216:219], v[72:75], v[112:115], v[216:219]
	v_mfma_f32_16x16x32_bf16 v[220:223], v[76:79], v[112:115], v[220:223]
	v_mfma_f32_16x16x32_bf16 v[224:227], v[80:83], v[112:115], v[224:227]
	v_mfma_f32_16x16x32_bf16 v[228:231], v[84:87], v[112:115], v[228:231]
	v_mfma_f32_16x16x32_bf16 v[232:235], v[72:75], v[116:119], v[232:235]
	v_mfma_f32_16x16x32_bf16 v[236:239], v[76:79], v[116:119], v[236:239]
	v_mfma_f32_16x16x32_bf16 v[240:243], v[80:83], v[116:119], v[240:243]
	v_mfma_f32_16x16x32_bf16 v[244:247], v[84:87], v[116:119], v[244:247]
	s_add_u32 s26, s26, 0x8000
	s_cmp_eq_u32 s26, s32
	s_cselect_b32 s26, s27, s26
	s_setprio 0
	s_barrier
	ds_read_b128 v[72:75], v6 offset:1024
	ds_read_b128 v[76:79], v6 offset:3072
	ds_read_b128 v[80:83], v6 offset:5120
	ds_read_b128 v[84:87], v6 offset:7168
	ds_read_b128 v[88:91], v4 offset:1024
	ds_read_b128 v[92:95], v4 offset:3072
	ds_read_b128 v[96:99], v4 offset:5120
	ds_read_b128 v[100:103], v4 offset:7168
	ds_read_b128 v[104:107], v4 offset:9216
	ds_read_b128 v[108:111], v4 offset:11264
	ds_read_b128 v[112:115], v4 offset:13312
	ds_read_b128 v[116:119], v4 offset:15360
	s_waitcnt vmcnt(22)
	v_cvt_pk_bf16_f32 v56, v56, v57
	v_cvt_pk_bf16_f32 v57, v58, v59
	v_cvt_pk_bf16_f32 v60, v60, v61
	v_cvt_pk_bf16_f32 v61, v62, v63
	ds_write2st64_b64 v3, v[56:57], v[60:61] offset0:96 offset1:104
	s_waitcnt vmcnt(20)
	v_cvt_pk_bf16_f32 v64, v64, v65
	v_cvt_pk_bf16_f32 v65, v66, v67
	v_cvt_pk_bf16_f32 v68, v68, v69
	v_cvt_pk_bf16_f32 v69, v70, v71
	ds_write2st64_b64 v3, v[64:65], v[68:69] offset0:112 offset1:120
	s_waitcnt vmcnt(16)
	s_waitcnt lgkmcnt(0)
	s_barrier
	s_setprio 1
	s_add_u32 s33, s33, 0x8000
	s_cmp_eq_u32 s33, 0x18000
	s_cselect_b32 s33, 0, s33
	s_add_u32 s25, s25, 1
	v_mfma_f32_16x16x32_bf16 v[120:123], v[72:75], v[88:91], v[120:123]
	v_mfma_f32_16x16x32_bf16 v[124:127], v[76:79], v[88:91], v[124:127]
	v_mfma_f32_16x16x32_bf16 v[128:131], v[80:83], v[88:91], v[128:131]
	v_mfma_f32_16x16x32_bf16 v[132:135], v[84:87], v[88:91], v[132:135]
	s_add_u32 s42, s41, 0x10000
	buffer_load_dwordx4 v[56:59], v1, s[4:7], s42 offen sc0 nt
	v_mfma_f32_16x16x32_bf16 v[136:139], v[72:75], v[92:95], v[136:139]
	v_mfma_f32_16x16x32_bf16 v[140:143], v[76:79], v[92:95], v[140:143]
	v_mfma_f32_16x16x32_bf16 v[144:147], v[80:83], v[92:95], v[144:147]
	v_mfma_f32_16x16x32_bf16 v[148:151], v[84:87], v[92:95], v[148:151]
	v_mfma_f32_16x16x32_bf16 v[152:155], v[72:75], v[96:99], v[152:155]
	v_mfma_f32_16x16x32_bf16 v[156:159], v[76:79], v[96:99], v[156:159]
	v_mfma_f32_16x16x32_bf16 v[160:163], v[80:83], v[96:99], v[160:163]
	v_mfma_f32_16x16x32_bf16 v[164:167], v[84:87], v[96:99], v[164:167]
	s_add_u32 s42, s41, 0x14000
	buffer_load_dwordx4 v[60:63], v1, s[4:7], s42 offen sc0 nt
	v_mfma_f32_16x16x32_bf16 v[168:171], v[72:75], v[100:103], v[168:171]
	v_mfma_f32_16x16x32_bf16 v[172:175], v[76:79], v[100:103], v[172:175]
	v_mfma_f32_16x16x32_bf16 v[176:179], v[80:83], v[100:103], v[176:179]
	v_mfma_f32_16x16x32_bf16 v[180:183], v[84:87], v[100:103], v[180:183]
	v_mfma_f32_16x16x32_bf16 v[184:187], v[72:75], v[104:107], v[184:187]
	v_mfma_f32_16x16x32_bf16 v[188:191], v[76:79], v[104:107], v[188:191]
	v_mfma_f32_16x16x32_bf16 v[192:195], v[80:83], v[104:107], v[192:195]
	v_mfma_f32_16x16x32_bf16 v[196:199], v[84:87], v[104:107], v[196:199]
	s_add_u32 s42, s41, 0x18000
	buffer_load_dwordx4 v[64:67], v1, s[4:7], s42 offen sc0 nt
	v_mfma_f32_16x16x32_bf16 v[200:203], v[72:75], v[108:111], v[200:203]
	v_mfma_f32_16x16x32_bf16 v[204:207], v[76:79], v[108:111], v[204:207]
	v_mfma_f32_16x16x32_bf16 v[208:211], v[80:83], v[108:111], v[208:211]
	v_mfma_f32_16x16x32_bf16 v[212:215], v[84:87], v[108:111], v[212:215]
	v_mfma_f32_16x16x32_bf16 v[216:219], v[72:75], v[112:115], v[216:219]
	v_mfma_f32_16x16x32_bf16 v[220:223], v[76:79], v[112:115], v[220:223]
	v_mfma_f32_16x16x32_bf16 v[224:227], v[80:83], v[112:115], v[224:227]
	v_mfma_f32_16x16x32_bf16 v[228:231], v[84:87], v[112:115], v[228:231]
	s_add_u32 s42, s41, 0x1c000
	buffer_load_dwordx4 v[68:71], v1, s[4:7], s42 offen sc0 nt
	v_mfma_f32_16x16x32_bf16 v[232:235], v[72:75], v[116:119], v[232:235]
	v_mfma_f32_16x16x32_bf16 v[236:239], v[76:79], v[116:119], v[236:239]
	v_mfma_f32_16x16x32_bf16 v[240:243], v[80:83], v[116:119], v[240:243]
	v_mfma_f32_16x16x32_bf16 v[244:247], v[84:87], v[116:119], v[244:247]
	s_setprio 0
	s_barrier
	v_add_u32_e32 v6, s33, v5
	ds_read_b128 v[72:75], v6 offset:0
	ds_read_b128 v[76:79], v6 offset:2048
	ds_read_b128 v[80:83], v6 offset:4096
	ds_read_b128 v[84:87], v6 offset:6144
	ds_read_b128 v[88:91], v4 offset:32768
	ds_read_b128 v[92:95], v4 offset:34816
	ds_read_b128 v[96:99], v4 offset:36864
	ds_read_b128 v[100:103], v4 offset:38912
	ds_read_b128 v[104:107], v4 offset:40960
	ds_read_b128 v[108:111], v4 offset:43008
	ds_read_b128 v[112:115], v4 offset:45056
	ds_read_b128 v[116:119], v4 offset:47104
	s_waitcnt vmcnt(18)
	v_cvt_pk_bf16_f32 v8, v8, v9
	v_cvt_pk_bf16_f32 v9, v10, v11
	v_cvt_pk_bf16_f32 v12, v12, v13
	v_cvt_pk_bf16_f32 v13, v14, v15
	ds_write2st64_b64 v3, v[8:9], v[12:13] offset0:0 offset1:8
	s_waitcnt vmcnt(16)
	v_cvt_pk_bf16_f32 v16, v16, v17
	v_cvt_pk_bf16_f32 v17, v18, v19
	v_cvt_pk_bf16_f32 v20, v20, v21
	v_cvt_pk_bf16_f32 v21, v22, v23
	ds_write2st64_b64 v3, v[16:17], v[20:21] offset0:16 offset1:24
	s_waitcnt lgkmcnt(0)
	s_barrier
	s_setprio 1
	s_mov_b32 m0, s26
	s_min_u32 s40, s25, 31
	s_bitcmp1_b32 s40, 4
	s_cselect_b32 s41, s23, s22
	s_lshl_b32 s42, s40, 23
	s_and_b32 s42, s42, 0x7000000
	s_or_b32 s41, s41, s42
	s_lshl_b32 s42, s40, 8
	s_and_b32 s42, s42, 0x100
	s_or_b32 s41, s41, s42
	s_sub_u32 s43, s25, 1
	s_min_u32 s43, s43, 31
	s_and_b32 s43, s43, 15
	s_lshl_b32 s43, s43, 15
	s_add_u32 s44, s43, s24
	v_mfma_f32_16x16x32_bf16 v[120:123], v[72:75], v[88:91], v[120:123]
	v_mfma_f32_16x16x32_bf16 v[124:127], v[76:79], v[88:91], v[124:127]
	buffer_load_dwordx4 v2, s[12:15], s44 offen sc1 lds
	v_mfma_f32_16x16x32_bf16 v[128:131], v[80:83], v[88:91], v[128:131]
	v_mfma_f32_16x16x32_bf16 v[132:135], v[84:87], v[88:91], v[132:135]
	buffer_load_dwordx4 v2, s[12:15], s44 offen offset:1024 sc1 lds
	v_mfma_f32_16x16x32_bf16 v[136:139], v[72:75], v[92:95], v[136:139]
	v_mfma_f32_16x16x32_bf16 v[140:143], v[76:79], v[92:95], v[140:143]
	buffer_load_dwordx4 v2, s[12:15], s44 offen offset:2048 sc1 lds
	v_mfma_f32_16x16x32_bf16 v[144:147], v[80:83], v[92:95], v[144:147]
	v_mfma_f32_16x16x32_bf16 v[148:151], v[84:87], v[92:95], v[148:151]
	buffer_load_dwordx4 v2, s[12:15], s44 offen offset:3072 sc1 lds
	v_mfma_f32_16x16x32_bf16 v[152:155], v[72:75], v[96:99], v[152:155]
	v_mfma_f32_16x16x32_bf16 v[156:159], v[76:79], v[96:99], v[156:159]
	v_mfma_f32_16x16x32_bf16 v[160:163], v[80:83], v[96:99], v[160:163]
	v_mfma_f32_16x16x32_bf16 v[164:167], v[84:87], v[96:99], v[164:167]
	buffer_load_dwordx4 v[8:11], v1, s[4:7], s41 offen sc0 nt
	v_mfma_f32_16x16x32_bf16 v[168:171], v[72:75], v[100:103], v[168:171]
	v_mfma_f32_16x16x32_bf16 v[172:175], v[76:79], v[100:103], v[172:175]
	v_mfma_f32_16x16x32_bf16 v[176:179], v[80:83], v[100:103], v[176:179]
	v_mfma_f32_16x16x32_bf16 v[180:183], v[84:87], v[100:103], v[180:183]
	s_add_u32 s42, s41, 0x4000
	buffer_load_dwordx4 v[12:15], v1, s[4:7], s42 offen sc0 nt
	v_mfma_f32_16x16x32_bf16 v[184:187], v[72:75], v[104:107], v[184:187]
	v_mfma_f32_16x16x32_bf16 v[188:191], v[76:79], v[104:107], v[188:191]
	v_mfma_f32_16x16x32_bf16 v[192:195], v[80:83], v[104:107], v[192:195]
	v_mfma_f32_16x16x32_bf16 v[196:199], v[84:87], v[104:107], v[196:199]
	s_add_u32 s42, s41, 0x8000
	buffer_load_dwordx4 v[16:19], v1, s[4:7], s42 offen sc0 nt
	v_mfma_f32_16x16x32_bf16 v[200:203], v[72:75], v[108:111], v[200:203]
	v_mfma_f32_16x16x32_bf16 v[204:207], v[76:79], v[108:111], v[204:207]
	v_mfma_f32_16x16x32_bf16 v[208:211], v[80:83], v[108:111], v[208:211]
	v_mfma_f32_16x16x32_bf16 v[212:215], v[84:87], v[108:111], v[212:215]
	s_add_u32 s42, s41, 0xc000
	buffer_load_dwordx4 v[20:23], v1, s[4:7], s42 offen sc0 nt
	v_mfma_f32_16x16x32_bf16 v[216:219], v[72:75], v[112:115], v[216:219]
	v_mfma_f32_16x16x32_bf16 v[220:223], v[76:79], v[112:115], v[220:223]
	v_mfma_f32_16x16x32_bf16 v[224:227], v[80:83], v[112:115], v[224:227]
	v_mfma_f32_16x16x32_bf16 v[228:231], v[84:87], v[112:115], v[228:231]
	v_mfma_f32_16x16x32_bf16 v[232:235], v[72:75], v[116:119], v[232:235]
	v_mfma_f32_16x16x32_bf16 v[236:239], v[76:79], v[116:119], v[236:239]
	v_mfma_f32_16x16x32_bf16 v[240:243], v[80:83], v[116:119], v[240:243]
	v_mfma_f32_16x16x32_bf16 v[244:247], v[84:87], v[116:119], v[244:247]
	s_add_u32 s26, s26, 0x8000
	s_cmp_eq_u32 s26, s32
	s_cselect_b32 s26, s27, s26
	s_setprio 0
	s_barrier
	ds_read_b128 v[72:75], v6 offset:1024
	ds_read_b128 v[76:79], v6 offset:3072
	ds_read_b128 v[80:83], v6 offset:5120
	ds_read_b128 v[84:87], v6 offset:7168
	ds_read_b128 v[88:91], v4 offset:33792
	ds_read_b128 v[92:95], v4 offset:35840
	ds_read_b128 v[96:99], v4 offset:37888
	ds_read_b128 v[100:103], v4 offset:39936
	ds_read_b128 v[104:107], v4 offset:41984
	ds_read_b128 v[108:111], v4 offset:44032
	ds_read_b128 v[112:115], v4 offset:46080
	ds_read_b128 v[116:119], v4 offset:48128
	s_waitcnt vmcnt(22)
	v_cvt_pk_bf16_f32 v24, v24, v25
	v_cvt_pk_bf16_f32 v25, v26, v27
	v_cvt_pk_bf16_f32 v28, v28, v29
	v_cvt_pk_bf16_f32 v29, v30, v31
	ds_write2st64_b64 v3, v[24:25], v[28:29] offset0:32 offset1:40
	s_waitcnt vmcnt(20)
	v_cvt_pk_bf16_f32 v32, v32, v33
	v_cvt_pk_bf16_f32 v33, v34, v35
	v_cvt_pk_bf16_f32 v36, v36, v37
	v_cvt_pk_bf16_f32 v37, v38, v39
	ds_write2st64_b64 v3, v[32:33], v[36:37] offset0:48 offset1:56
	s_waitcnt vmcnt(16)
	s_waitcnt lgkmcnt(0)
	s_barrier
	s_setprio 1
	s_add_u32 s33, s33, 0x8000
	s_cmp_eq_u32 s33, 0x18000
	s_cselect_b32 s33, 0, s33
	s_add_u32 s25, s25, 1
	v_mfma_f32_16x16x32_bf16 v[120:123], v[72:75], v[88:91], v[120:123]
	v_mfma_f32_16x16x32_bf16 v[124:127], v[76:79], v[88:91], v[124:127]
	v_mfma_f32_16x16x32_bf16 v[128:131], v[80:83], v[88:91], v[128:131]
	v_mfma_f32_16x16x32_bf16 v[132:135], v[84:87], v[88:91], v[132:135]
	s_add_u32 s42, s41, 0x10000
	buffer_load_dwordx4 v[24:27], v1, s[4:7], s42 offen sc0 nt
	v_mfma_f32_16x16x32_bf16 v[136:139], v[72:75], v[92:95], v[136:139]
	v_mfma_f32_16x16x32_bf16 v[140:143], v[76:79], v[92:95], v[140:143]
	v_mfma_f32_16x16x32_bf16 v[144:147], v[80:83], v[92:95], v[144:147]
	v_mfma_f32_16x16x32_bf16 v[148:151], v[84:87], v[92:95], v[148:151]
	v_mfma_f32_16x16x32_bf16 v[152:155], v[72:75], v[96:99], v[152:155]
	v_mfma_f32_16x16x32_bf16 v[156:159], v[76:79], v[96:99], v[156:159]
	v_mfma_f32_16x16x32_bf16 v[160:163], v[80:83], v[96:99], v[160:163]
	v_mfma_f32_16x16x32_bf16 v[164:167], v[84:87], v[96:99], v[164:167]
	s_add_u32 s42, s41, 0x14000
	buffer_load_dwordx4 v[28:31], v1, s[4:7], s42 offen sc0 nt
	v_mfma_f32_16x16x32_bf16 v[168:171], v[72:75], v[100:103], v[168:171]
	v_mfma_f32_16x16x32_bf16 v[172:175], v[76:79], v[100:103], v[172:175]
	v_mfma_f32_16x16x32_bf16 v[176:179], v[80:83], v[100:103], v[176:179]
	v_mfma_f32_16x16x32_bf16 v[180:183], v[84:87], v[100:103], v[180:183]
	v_mfma_f32_16x16x32_bf16 v[184:187], v[72:75], v[104:107], v[184:187]
	v_mfma_f32_16x16x32_bf16 v[188:191], v[76:79], v[104:107], v[188:191]
	v_mfma_f32_16x16x32_bf16 v[192:195], v[80:83], v[104:107], v[192:195]
	v_mfma_f32_16x16x32_bf16 v[196:199], v[84:87], v[104:107], v[196:199]
	s_add_u32 s42, s41, 0x18000
	buffer_load_dwordx4 v[32:35], v1, s[4:7], s42 offen sc0 nt
	v_mfma_f32_16x16x32_bf16 v[200:203], v[72:75], v[108:111], v[200:203]
	v_mfma_f32_16x16x32_bf16 v[204:207], v[76:79], v[108:111], v[204:207]
	v_mfma_f32_16x16x32_bf16 v[208:211], v[80:83], v[108:111], v[208:211]
	v_mfma_f32_16x16x32_bf16 v[212:215], v[84:87], v[108:111], v[212:215]
	v_mfma_f32_16x16x32_bf16 v[216:219], v[72:75], v[112:115], v[216:219]
	v_mfma_f32_16x16x32_bf16 v[220:223], v[76:79], v[112:115], v[220:223]
	v_mfma_f32_16x16x32_bf16 v[224:227], v[80:83], v[112:115], v[224:227]
	v_mfma_f32_16x16x32_bf16 v[228:231], v[84:87], v[112:115], v[228:231]
	s_add_u32 s42, s41, 0x1c000
	buffer_load_dwordx4 v[36:39], v1, s[4:7], s42 offen sc0 nt
	v_mfma_f32_16x16x32_bf16 v[232:235], v[72:75], v[116:119], v[232:235]
	v_mfma_f32_16x16x32_bf16 v[236:239], v[76:79], v[116:119], v[236:239]
	v_mfma_f32_16x16x32_bf16 v[240:243], v[80:83], v[116:119], v[240:243]
	v_mfma_f32_16x16x32_bf16 v[244:247], v[84:87], v[116:119], v[244:247]
	s_setprio 0
	s_barrier
	s_sub_u32 s38, s38, 1
	s_cmp_lg_u32 s38, 0
	s_cbranch_scc1 .Lg_loop
	s_cmp_lg_u32 s39, 0
	s_cbranch_scc1 .Lg_final
	v_add_u32_e32 v6, s33, v5
	ds_read_b128 v[72:75], v6 offset:0
	ds_read_b128 v[76:79], v6 offset:2048
	ds_read_b128 v[80:83], v6 offset:4096
	ds_read_b128 v[84:87], v6 offset:6144
	ds_read_b128 v[88:91], v4 offset:0
	ds_read_b128 v[92:95], v4 offset:2048
	ds_read_b128 v[96:99], v4 offset:4096
	ds_read_b128 v[100:103], v4 offset:6144
	ds_read_b128 v[104:107], v4 offset:8192
	ds_read_b128 v[108:111], v4 offset:10240
	ds_read_b128 v[112:115], v4 offset:12288
	ds_read_b128 v[116:119], v4 offset:14336
	s_waitcnt vmcnt(18)
	v_cvt_pk_bf16_f32 v40, v40, v41
	v_cvt_pk_bf16_f32 v41, v42, v43
	v_cvt_pk_bf16_f32 v44, v44, v45
	v_cvt_pk_bf16_f32 v45, v46, v47
	ds_write2st64_b64 v3, v[40:41], v[44:45] offset0:64 offset1:72
	s_waitcnt vmcnt(16)
	v_cvt_pk_bf16_f32 v48, v48, v49
	v_cvt_pk_bf16_f32 v49, v50, v51
	v_cvt_pk_bf16_f32 v52, v52, v53
	v_cvt_pk_bf16_f32 v53, v54, v55
	ds_write2st64_b64 v3, v[48:49], v[52:53] offset0:80 offset1:88
	s_waitcnt lgkmcnt(0)
	global_load_dwordx4 v[40:43], v249, s[34:35] offset:0
	global_load_dwordx4 v[44:47], v249, s[34:35] offset:64
	global_load_dwordx4 v[48:51], v249, s[34:35] offset:128
	global_load_dwordx4 v[52:55], v249, s[34:35] offset:192
	s_barrier
	s_setprio 1
	s_mov_b32 m0, s26
	s_min_u32 s40, s25, 31
	s_bitcmp1_b32 s40, 4
	s_cselect_b32 s41, s23, s22
	s_lshl_b32 s42, s40, 23
	s_and_b32 s42, s42, 0x7000000
	s_or_b32 s41, s41, s42
	s_lshl_b32 s42, s40, 8
	s_and_b32 s42, s42, 0x100
	s_or_b32 s41, s41, s42
	s_sub_u32 s43, s25, 1
	s_min_u32 s43, s43, 31
	s_and_b32 s43, s43, 15
	s_lshl_b32 s43, s43, 15
	s_add_u32 s44, s43, s24
	buffer_load_dwordx4 v2, s[12:15], s44 offen sc1 lds
	buffer_load_dwordx4 v2, s[12:15], s44 offen offset:1024 sc1 lds
	buffer_load_dwordx4 v2, s[12:15], s44 offen offset:2048 sc1 lds
	buffer_load_dwordx4 v2, s[12:15], s44 offen offset:3072 sc1 lds
	s_waitcnt vmcnt(4)
	s_mov_b32 s45, s36
	buffer_store_dwordx4 v[120:123], v248, s[28:31], s45 offen
	buffer_store_dwordx4 v[124:127], v248, s[28:31], s45 offen offset:64
	v_mfma_f32_16x16x32_bf16 v[120:123], v[72:75], v[88:91], v[40:43]
	buffer_store_dwordx4 v[128:131], v248, s[28:31], s45 offen offset:128
	v_mfma_f32_16x16x32_bf16 v[124:127], v[76:79], v[88:91], v[44:47]
	buffer_store_dwordx4 v[132:135], v248, s[28:31], s45 offen offset:192
	v_mfma_f32_16x16x32_bf16 v[128:131], v[80:83], v[88:91], v[48:51]
	s_add_u32 s45, s36, 0x2000
	buffer_store_dwordx4 v[136:139], v248, s[28:31], s45 offen
	v_mfma_f32_16x16x32_bf16 v[132:135], v[84:87], v[88:91], v[52:55]
	buffer_store_dwordx4 v[140:143], v248, s[28:31], s45 offen offset:64
	v_mfma_f32_16x16x32_bf16 v[136:139], v[72:75], v[92:95], v[40:43]
	buffer_store_dwordx4 v[144:147], v248, s[28:31], s45 offen offset:128
	v_mfma_f32_16x16x32_bf16 v[140:143], v[76:79], v[92:95], v[44:47]
	buffer_store_dwordx4 v[148:151], v248, s[28:31], s45 offen offset:192
	v_mfma_f32_16x16x32_bf16 v[144:147], v[80:83], v[92:95], v[48:51]
	s_add_u32 s45, s36, 0x4000
	buffer_store_dwordx4 v[152:155], v248, s[28:31], s45 offen
	v_mfma_f32_16x16x32_bf16 v[148:151], v[84:87], v[92:95], v[52:55]
	buffer_store_dwordx4 v[156:159], v248, s[28:31], s45 offen offset:64
	v_mfma_f32_16x16x32_bf16 v[152:155], v[72:75], v[96:99], v[40:43]
	buffer_store_dwordx4 v[160:163], v248, s[28:31], s45 offen offset:128
	v_mfma_f32_16x16x32_bf16 v[156:159], v[76:79], v[96:99], v[44:47]
	buffer_store_dwordx4 v[164:167], v248, s[28:31], s45 offen offset:192
	v_mfma_f32_16x16x32_bf16 v[160:163], v[80:83], v[96:99], v[48:51]
	s_add_u32 s45, s36, 0x6000
	buffer_store_dwordx4 v[168:171], v248, s[28:31], s45 offen
	v_mfma_f32_16x16x32_bf16 v[164:167], v[84:87], v[96:99], v[52:55]
	buffer_store_dwordx4 v[172:175], v248, s[28:31], s45 offen offset:64
	v_mfma_f32_16x16x32_bf16 v[168:171], v[72:75], v[100:103], v[40:43]
	buffer_store_dwordx4 v[176:179], v248, s[28:31], s45 offen offset:128
	v_mfma_f32_16x16x32_bf16 v[172:175], v[76:79], v[100:103], v[44:47]
	buffer_store_dwordx4 v[180:183], v248, s[28:31], s45 offen offset:192
	v_mfma_f32_16x16x32_bf16 v[176:179], v[80:83], v[100:103], v[48:51]
	s_add_u32 s45, s36, 0x8000
	buffer_store_dwordx4 v[184:187], v248, s[28:31], s45 offen
	v_mfma_f32_16x16x32_bf16 v[180:183], v[84:87], v[100:103], v[52:55]
	buffer_store_dwordx4 v[188:191], v248, s[28:31], s45 offen offset:64
	v_mfma_f32_16x16x32_bf16 v[184:187], v[72:75], v[104:107], v[40:43]
	buffer_store_dwordx4 v[192:195], v248, s[28:31], s45 offen offset:128
	v_mfma_f32_16x16x32_bf16 v[188:191], v[76:79], v[104:107], v[44:47]
	buffer_store_dwordx4 v[196:199], v248, s[28:31], s45 offen offset:192
	v_mfma_f32_16x16x32_bf16 v[192:195], v[80:83], v[104:107], v[48:51]
	s_add_u32 s45, s36, 0xa000
	buffer_store_dwordx4 v[200:203], v248, s[28:31], s45 offen
	v_mfma_f32_16x16x32_bf16 v[196:199], v[84:87], v[104:107], v[52:55]
	buffer_store_dwordx4 v[204:207], v248, s[28:31], s45 offen offset:64
	v_mfma_f32_16x16x32_bf16 v[200:203], v[72:75], v[108:111], v[40:43]
	buffer_store_dwordx4 v[208:211], v248, s[28:31], s45 offen offset:128
	v_mfma_f32_16x16x32_bf16 v[204:207], v[76:79], v[108:111], v[44:47]
	buffer_store_dwordx4 v[212:215], v248, s[28:31], s45 offen offset:192
	v_mfma_f32_16x16x32_bf16 v[208:211], v[80:83], v[108:111], v[48:51]
	s_add_u32 s45, s36, 0xc000
	buffer_store_dwordx4 v[216:219], v248, s[28:31], s45 offen
	v_mfma_f32_16x16x32_bf16 v[212:215], v[84:87], v[108:111], v[52:55]
	buffer_store_dwordx4 v[220:223], v248, s[28:31], s45 offen offset:64
	v_mfma_f32_16x16x32_bf16 v[216:219], v[72:75], v[112:115], v[40:43]
	buffer_store_dwordx4 v[224:227], v248, s[28:31], s45 offen offset:128
	v_mfma_f32_16x16x32_bf16 v[220:223], v[76:79], v[112:115], v[44:47]
	buffer_store_dwordx4 v[228:231], v248, s[28:31], s45 offen offset:192
	v_mfma_f32_16x16x32_bf16 v[224:227], v[80:83], v[112:115], v[48:51]
	s_add_u32 s45, s36, 0xe000
	buffer_store_dwordx4 v[232:235], v248, s[28:31], s45 offen
	v_mfma_f32_16x16x32_bf16 v[228:231], v[84:87], v[112:115], v[52:55]
	buffer_store_dwordx4 v[236:239], v248, s[28:31], s45 offen offset:64
	v_mfma_f32_16x16x32_bf16 v[232:235], v[72:75], v[116:119], v[40:43]
	buffer_store_dwordx4 v[240:243], v248, s[28:31], s45 offen offset:128
	v_mfma_f32_16x16x32_bf16 v[236:239], v[76:79], v[116:119], v[44:47]
	buffer_store_dwordx4 v[244:247], v248, s[28:31], s45 offen offset:192
	v_mfma_f32_16x16x32_bf16 v[240:243], v[80:83], v[116:119], v[48:51]
	v_mfma_f32_16x16x32_bf16 v[244:247], v[84:87], v[116:119], v[52:55]
	s_add_u32 s26, s26, 0x8000
	s_cmp_eq_u32 s26, s32
	s_cselect_b32 s26, s27, s26
	s_setprio 0
	s_barrier
	ds_read_b128 v[72:75], v6 offset:1024
	ds_read_b128 v[76:79], v6 offset:3072
	ds_read_b128 v[80:83], v6 offset:5120
	ds_read_b128 v[84:87], v6 offset:7168
	ds_read_b128 v[88:91], v4 offset:1024
	ds_read_b128 v[92:95], v4 offset:3072
	ds_read_b128 v[96:99], v4 offset:5120
	ds_read_b128 v[100:103], v4 offset:7168
	ds_read_b128 v[104:107], v4 offset:9216
	ds_read_b128 v[108:111], v4 offset:11264
	ds_read_b128 v[112:115], v4 offset:13312
	ds_read_b128 v[116:119], v4 offset:15360
	s_waitcnt vmcnt(54)
	v_cvt_pk_bf16_f32 v56, v56, v57
	v_cvt_pk_bf16_f32 v57, v58, v59
	v_cvt_pk_bf16_f32 v60, v60, v61
	v_cvt_pk_bf16_f32 v61, v62, v63
	ds_write2st64_b64 v3, v[56:57], v[60:61] offset0:96 offset1:104
	s_waitcnt vmcnt(52)
	v_cvt_pk_bf16_f32 v64, v64, v65
	v_cvt_pk_bf16_f32 v65, v66, v67
	v_cvt_pk_bf16_f32 v68, v68, v69
	v_cvt_pk_bf16_f32 v69, v70, v71
	ds_write2st64_b64 v3, v[64:65], v[68:69] offset0:112 offset1:120
	s_waitcnt vmcnt(48)
	s_waitcnt lgkmcnt(0)
	s_barrier
	s_setprio 1
	s_add_u32 s33, s33, 0x8000
	s_cmp_eq_u32 s33, 0x18000
	s_cselect_b32 s33, 0, s33
	s_add_u32 s25, s25, 1
	v_mfma_f32_16x16x32_bf16 v[120:123], v[72:75], v[88:91], v[120:123]
	v_mfma_f32_16x16x32_bf16 v[124:127], v[76:79], v[88:91], v[124:127]
	v_mfma_f32_16x16x32_bf16 v[128:131], v[80:83], v[88:91], v[128:131]
	buffer_load_dwordx4 v[40:43], v1, s[4:7], s41 offen sc0 nt
	v_mfma_f32_16x16x32_bf16 v[132:135], v[84:87], v[88:91], v[132:135]
	v_mfma_f32_16x16x32_bf16 v[136:139], v[72:75], v[92:95], v[136:139]
	v_mfma_f32_16x16x32_bf16 v[140:143], v[76:79], v[92:95], v[140:143]
	v_mfma_f32_16x16x32_bf16 v[144:147], v[80:83], v[92:95], v[144:147]
	s_add_u32 s42, s41, 0x4000
	buffer_load_dwordx4 v[44:47], v1, s[4:7], s42 offen sc0 nt
	v_mfma_f32_16x16x32_bf16 v[148:151], v[84:87], v[92:95], v[148:151]
	v_mfma_f32_16x16x32_bf16 v[152:155], v[72:75], v[96:99], v[152:155]
	v_mfma_f32_16x16x32_bf16 v[156:159], v[76:79], v[96:99], v[156:159]
	v_mfma_f32_16x16x32_bf16 v[160:163], v[80:83], v[96:99], v[160:163]
	s_add_u32 s42, s41, 0x8000
	buffer_load_dwordx4 v[48:51], v1, s[4:7], s42 offen sc0 nt
	v_mfma_f32_16x16x32_bf16 v[164:167], v[84:87], v[96:99], v[164:167]
	v_mfma_f32_16x16x32_bf16 v[168:171], v[72:75], v[100:103], v[168:171]
	v_mfma_f32_16x16x32_bf16 v[172:175], v[76:79], v[100:103], v[172:175]
	v_mfma_f32_16x16x32_bf16 v[176:179], v[80:83], v[100:103], v[176:179]
	s_add_u32 s42, s41, 0xc000
	buffer_load_dwordx4 v[52:55], v1, s[4:7], s42 offen sc0 nt
	v_mfma_f32_16x16x32_bf16 v[180:183], v[84:87], v[100:103], v[180:183]
	v_mfma_f32_16x16x32_bf16 v[184:187], v[72:75], v[104:107], v[184:187]
	v_mfma_f32_16x16x32_bf16 v[188:191], v[76:79], v[104:107], v[188:191]
	v_mfma_f32_16x16x32_bf16 v[192:195], v[80:83], v[104:107], v[192:195]
	s_add_u32 s42, s41, 0x10000
	buffer_load_dwordx4 v[56:59], v1, s[4:7], s42 offen sc0 nt
	v_mfma_f32_16x16x32_bf16 v[196:199], v[84:87], v[104:107], v[196:199]
	v_mfma_f32_16x16x32_bf16 v[200:203], v[72:75], v[108:111], v[200:203]
	v_mfma_f32_16x16x32_bf16 v[204:207], v[76:79], v[108:111], v[204:207]
	v_mfma_f32_16x16x32_bf16 v[208:211], v[80:83], v[108:111], v[208:211]
	s_add_u32 s42, s41, 0x14000
	buffer_load_dwordx4 v[60:63], v1, s[4:7], s42 offen sc0 nt
	v_mfma_f32_16x16x32_bf16 v[212:215], v[84:87], v[108:111], v[212:215]
	v_mfma_f32_16x16x32_bf16 v[216:219], v[72:75], v[112:115], v[216:219]
	v_mfma_f32_16x16x32_bf16 v[220:223], v[76:79], v[112:115], v[220:223]
	v_mfma_f32_16x16x32_bf16 v[224:227], v[80:83], v[112:115], v[224:227]
	s_add_u32 s42, s41, 0x18000
	buffer_load_dwordx4 v[64:67], v1, s[4:7], s42 offen sc0 nt
	v_mfma_f32_16x16x32_bf16 v[228:231], v[84:87], v[112:115], v[228:231]
	v_mfma_f32_16x16x32_bf16 v[232:235], v[72:75], v[116:119], v[232:235]
	v_mfma_f32_16x16x32_bf16 v[236:239], v[76:79], v[116:119], v[236:239]
	v_mfma_f32_16x16x32_bf16 v[240:243], v[80:83], v[116:119], v[240:243]
	s_add_u32 s42, s41, 0x1c000
	buffer_load_dwordx4 v[68:71], v1, s[4:7], s42 offen sc0 nt
	v_mfma_f32_16x16x32_bf16 v[244:247], v[84:87], v[116:119], v[244:247]
	s_setprio 0
	s_barrier
	v_add_u32_e32 v6, s33, v5
	ds_read_b128 v[72:75], v6 offset:0
	ds_read_b128 v[76:79], v6 offset:2048
	ds_read_b128 v[80:83], v6 offset:4096
	ds_read_b128 v[84:87], v6 offset:6144
	ds_read_b128 v[88:91], v4 offset:32768
	ds_read_b128 v[92:95], v4 offset:34816
	ds_read_b128 v[96:99], v4 offset:36864
	ds_read_b128 v[100:103], v4 offset:38912
	ds_read_b128 v[104:107], v4 offset:40960
	ds_read_b128 v[108:111], v4 offset:43008
	ds_read_b128 v[112:115], v4 offset:45056
	ds_read_b128 v[116:119], v4 offset:47104
	s_waitcnt vmcnt(54)
	v_cvt_pk_bf16_f32 v8, v8, v9
	v_cvt_pk_bf16_f32 v9, v10, v11
	v_cvt_pk_bf16_f32 v12, v12, v13
	v_cvt_pk_bf16_f32 v13, v14, v15
	ds_write2st64_b64 v3, v[8:9], v[12:13] offset0:0 offset1:8
	s_waitcnt vmcnt(52)
	v_cvt_pk_bf16_f32 v16, v16, v17
	v_cvt_pk_bf16_f32 v17, v18, v19
	v_cvt_pk_bf16_f32 v20, v20, v21
	v_cvt_pk_bf16_f32 v21, v22, v23
	ds_write2st64_b64 v3, v[16:17], v[20:21] offset0:16 offset1:24
	s_waitcnt lgkmcnt(0)
	s_barrier
	s_setprio 1
	s_mov_b32 m0, s26
	s_min_u32 s40, s25, 31
	s_bitcmp1_b32 s40, 4
	s_cselect_b32 s41, s23, s22
	s_lshl_b32 s42, s40, 23
	s_and_b32 s42, s42, 0x7000000
	s_or_b32 s41, s41, s42
	s_lshl_b32 s42, s40, 8
	s_and_b32 s42, s42, 0x100
	s_or_b32 s41, s41, s42
	s_sub_u32 s43, s25, 1
	s_min_u32 s43, s43, 31
	s_and_b32 s43, s43, 15
	s_lshl_b32 s43, s43, 15
	s_add_u32 s44, s43, s24
	v_mfma_f32_16x16x32_bf16 v[120:123], v[72:75], v[88:91], v[120:123]
	v_mfma_f32_16x16x32_bf16 v[124:127], v[76:79], v[88:91], v[124:127]
	buffer_load_dwordx4 v2, s[12:15], s44 offen sc1 lds
	v_mfma_f32_16x16x32_bf16 v[128:131], v[80:83], v[88:91], v[128:131]
	v_mfma_f32_16x16x32_bf16 v[132:135], v[84:87], v[88:91], v[132:135]
	buffer_load_dwordx4 v2, s[12:15], s44 offen offset:1024 sc1 lds
	v_mfma_f32_16x16x32_bf16 v[136:139], v[72:75], v[92:95], v[136:139]
	v_mfma_f32_16x16x32_bf16 v[140:143], v[76:79], v[92:95], v[140:143]
	buffer_load_dwordx4 v2, s[12:15], s44 offen offset:2048 sc1 lds
	v_mfma_f32_16x16x32_bf16 v[144:147], v[80:83], v[92:95], v[144:147]
	v_mfma_f32_16x16x32_bf16 v[148:151], v[84:87], v[92:95], v[148:151]
	buffer_load_dwordx4 v2, s[12:15], s44 offen offset:3072 sc1 lds
	v_mfma_f32_16x16x32_bf16 v[152:155], v[72:75], v[96:99], v[152:155]
	v_mfma_f32_16x16x32_bf16 v[156:159], v[76:79], v[96:99], v[156:159]
	v_mfma_f32_16x16x32_bf16 v[160:163], v[80:83], v[96:99], v[160:163]
	v_mfma_f32_16x16x32_bf16 v[164:167], v[84:87], v[96:99], v[164:167]
	buffer_load_dwordx4 v[8:11], v1, s[4:7], s41 offen sc0 nt
	v_mfma_f32_16x16x32_bf16 v[168:171], v[72:75], v[100:103], v[168:171]
	v_mfma_f32_16x16x32_bf16 v[172:175], v[76:79], v[100:103], v[172:175]
	v_mfma_f32_16x16x32_bf16 v[176:179], v[80:83], v[100:103], v[176:179]
	v_mfma_f32_16x16x32_bf16 v[180:183], v[84:87], v[100:103], v[180:183]
	s_add_u32 s42, s41, 0x4000
	buffer_load_dwordx4 v[12:15], v1, s[4:7], s42 offen sc0 nt
	v_mfma_f32_16x16x32_bf16 v[184:187], v[72:75], v[104:107], v[184:187]
	v_mfma_f32_16x16x32_bf16 v[188:191], v[76:79], v[104:107], v[188:191]
	v_mfma_f32_16x16x32_bf16 v[192:195], v[80:83], v[104:107], v[192:195]
	v_mfma_f32_16x16x32_bf16 v[196:199], v[84:87], v[104:107], v[196:199]
	s_add_u32 s42, s41, 0x8000
	buffer_load_dwordx4 v[16:19], v1, s[4:7], s42 offen sc0 nt
	v_mfma_f32_16x16x32_bf16 v[200:203], v[72:75], v[108:111], v[200:203]
	v_mfma_f32_16x16x32_bf16 v[204:207], v[76:79], v[108:111], v[204:207]
	v_mfma_f32_16x16x32_bf16 v[208:211], v[80:83], v[108:111], v[208:211]
	v_mfma_f32_16x16x32_bf16 v[212:215], v[84:87], v[108:111], v[212:215]
	s_add_u32 s42, s41, 0xc000
	buffer_load_dwordx4 v[20:23], v1, s[4:7], s42 offen sc0 nt
	v_mfma_f32_16x16x32_bf16 v[216:219], v[72:75], v[112:115], v[216:219]
	v_mfma_f32_16x16x32_bf16 v[220:223], v[76:79], v[112:115], v[220:223]
	v_mfma_f32_16x16x32_bf16 v[224:227], v[80:83], v[112:115], v[224:227]
	v_mfma_f32_16x16x32_bf16 v[228:231], v[84:87], v[112:115], v[228:231]
	v_mfma_f32_16x16x32_bf16 v[232:235], v[72:75], v[116:119], v[232:235]
	v_mfma_f32_16x16x32_bf16 v[236:239], v[76:79], v[116:119], v[236:239]
	v_mfma_f32_16x16x32_bf16 v[240:243], v[80:83], v[116:119], v[240:243]
	v_mfma_f32_16x16x32_bf16 v[244:247], v[84:87], v[116:119], v[244:247]
	s_add_u32 s26, s26, 0x8000
	s_cmp_eq_u32 s26, s32
	s_cselect_b32 s26, s27, s26
	s_setprio 0
	s_barrier
	ds_read_b128 v[72:75], v6 offset:1024
	ds_read_b128 v[76:79], v6 offset:3072
	ds_read_b128 v[80:83], v6 offset:5120
	ds_read_b128 v[84:87], v6 offset:7168
	ds_read_b128 v[88:91], v4 offset:33792
	ds_read_b128 v[92:95], v4 offset:35840
	ds_read_b128 v[96:99], v4 offset:37888
	ds_read_b128 v[100:103], v4 offset:39936
	ds_read_b128 v[104:107], v4 offset:41984
	ds_read_b128 v[108:111], v4 offset:44032
	ds_read_b128 v[112:115], v4 offset:46080
	ds_read_b128 v[116:119], v4 offset:48128
	s_waitcnt vmcnt(58)
	v_cvt_pk_bf16_f32 v24, v24, v25
	v_cvt_pk_bf16_f32 v25, v26, v27
	v_cvt_pk_bf16_f32 v28, v28, v29
	v_cvt_pk_bf16_f32 v29, v30, v31
	ds_write2st64_b64 v3, v[24:25], v[28:29] offset0:32 offset1:40
	s_waitcnt vmcnt(56)
	v_cvt_pk_bf16_f32 v32, v32, v33
	v_cvt_pk_bf16_f32 v33, v34, v35
	v_cvt_pk_bf16_f32 v36, v36, v37
	v_cvt_pk_bf16_f32 v37, v38, v39
	ds_write2st64_b64 v3, v[32:33], v[36:37] offset0:48 offset1:56
	s_waitcnt vmcnt(48)
	s_waitcnt lgkmcnt(0)
	s_barrier
	s_setprio 1
	s_add_u32 s33, s33, 0x8000
	s_cmp_eq_u32 s33, 0x18000
	s_cselect_b32 s33, 0, s33
	s_add_u32 s25, s25, 1
	v_mfma_f32_16x16x32_bf16 v[120:123], v[72:75], v[88:91], v[120:123]
	v_mfma_f32_16x16x32_bf16 v[124:127], v[76:79], v[88:91], v[124:127]
	v_mfma_f32_16x16x32_bf16 v[128:131], v[80:83], v[88:91], v[128:131]
	v_mfma_f32_16x16x32_bf16 v[132:135], v[84:87], v[88:91], v[132:135]
	s_add_u32 s42, s41, 0x10000
	buffer_load_dwordx4 v[24:27], v1, s[4:7], s42 offen sc0 nt
	v_mfma_f32_16x16x32_bf16 v[136:139], v[72:75], v[92:95], v[136:139]
	v_mfma_f32_16x16x32_bf16 v[140:143], v[76:79], v[92:95], v[140:143]
	v_mfma_f32_16x16x32_bf16 v[144:147], v[80:83], v[92:95], v[144:147]
	v_mfma_f32_16x16x32_bf16 v[148:151], v[84:87], v[92:95], v[148:151]
	v_mfma_f32_16x16x32_bf16 v[152:155], v[72:75], v[96:99], v[152:155]
	v_mfma_f32_16x16x32_bf16 v[156:159], v[76:79], v[96:99], v[156:159]
	v_mfma_f32_16x16x32_bf16 v[160:163], v[80:83], v[96:99], v[160:163]
	v_mfma_f32_16x16x32_bf16 v[164:167], v[84:87], v[96:99], v[164:167]
	s_add_u32 s42, s41, 0x14000
	buffer_load_dwordx4 v[28:31], v1, s[4:7], s42 offen sc0 nt
	v_mfma_f32_16x16x32_bf16 v[168:171], v[72:75], v[100:103], v[168:171]
	v_mfma_f32_16x16x32_bf16 v[172:175], v[76:79], v[100:103], v[172:175]
	v_mfma_f32_16x16x32_bf16 v[176:179], v[80:83], v[100:103], v[176:179]
	v_mfma_f32_16x16x32_bf16 v[180:183], v[84:87], v[100:103], v[180:183]
	v_mfma_f32_16x16x32_bf16 v[184:187], v[72:75], v[104:107], v[184:187]
	v_mfma_f32_16x16x32_bf16 v[188:191], v[76:79], v[104:107], v[188:191]
	v_mfma_f32_16x16x32_bf16 v[192:195], v[80:83], v[104:107], v[192:195]
	v_mfma_f32_16x16x32_bf16 v[196:199], v[84:87], v[104:107], v[196:199]
	s_add_u32 s42, s41, 0x18000
	buffer_load_dwordx4 v[32:35], v1, s[4:7], s42 offen sc0 nt
	v_mfma_f32_16x16x32_bf16 v[200:203], v[72:75], v[108:111], v[200:203]
	v_mfma_f32_16x16x32_bf16 v[204:207], v[76:79], v[108:111], v[204:207]
	v_mfma_f32_16x16x32_bf16 v[208:211], v[80:83], v[108:111], v[208:211]
	v_mfma_f32_16x16x32_bf16 v[212:215], v[84:87], v[108:111], v[212:215]
	v_mfma_f32_16x16x32_bf16 v[216:219], v[72:75], v[112:115], v[216:219]
	v_mfma_f32_16x16x32_bf16 v[220:223], v[76:79], v[112:115], v[220:223]
	v_mfma_f32_16x16x32_bf16 v[224:227], v[80:83], v[112:115], v[224:227]
	v_mfma_f32_16x16x32_bf16 v[228:231], v[84:87], v[112:115], v[228:231]
	s_add_u32 s42, s41, 0x1c000
	buffer_load_dwordx4 v[36:39], v1, s[4:7], s42 offen sc0 nt
	v_mfma_f32_16x16x32_bf16 v[232:235], v[72:75], v[116:119], v[232:235]
	v_mfma_f32_16x16x32_bf16 v[236:239], v[76:79], v[116:119], v[236:239]
	v_mfma_f32_16x16x32_bf16 v[240:243], v[80:83], v[116:119], v[240:243]
	v_mfma_f32_16x16x32_bf16 v[244:247], v[84:87], v[116:119], v[244:247]
	s_setprio 0
	s_barrier
	s_mov_b32 s39, 1
	s_mov_b32 s38, 7
	s_branch .Lg_loop
